# early acquire-invalidate also at the stick-breaking -> out-projection barrier
# baseline (speedup 1.0000x reference)
; __device__ __forceinline__ unsigned xb_ld(unsigned* p)              { return __hip_atomic_load(p, __ATOMIC_RELAXED, __HIP_MEMORY_SCOPE_AGENT); }
; __device__ __forceinline__ unsigned xb_add(unsigned* p, unsigned v) { return __hip_atomic_fetch_add(p, v, __ATOMIC_RELAXED, __HIP_MEMORY_SCOPE_AGENT); }
; #define XB_SPIN(cond, bar) do { unsigned _sp = 0; while (cond) { __builtin_amdgcn_s_sleep(1); \
;     if ((++_sp & 255u) == 0u) { if (xb_ld(&(bar)[XB_TMO])) break; if (_sp > XB_SPIN_CAP) { atomicAdd(&(bar)[XB_TMO], 1u); break; } } } } while (0)
; __device__ __forceinline__ void xcd_barrier_impl(const XcdBarrier& b, bool leader) {
;     ...
;         const unsigned old = xb_add(&bar[XB_XSUB(b.x)], 1u);
;         const unsigned gen = old / nloc;
;         if (old + 1u == (gen + 1u) * nloc) {
;             __builtin_amdgcn_fence(__ATOMIC_RELEASE, "agent");
;             asm volatile("s_waitcnt vmcnt(0)" ::: "memory");
;             const unsigned og = xb_add(&bar[XB_TOP], 1u);
;             const unsigned tg = og / nx;
;             if (og + 1u != (tg + 1u) * nx) XB_SPIN(xb_ld(&bar[XB_TOP]) < (tg + 1u) * nx, bar);
.LBB0_393:
	s_or_b64 exec, exec, s[8:9]
	buffer_inv sc1
	v_cvt_f32_u32_e32 v5, v2
	s_waitcnt vmcnt(1)
	v_readfirstlane_b32 s0, v4
	v_sub_u32_e32 v4, 0, v2
	v_rcp_iflag_f32_e32 v5, v5
	v_add_u32_e32 v3, s0, v3
	v_mul_f32_e32 v5, 0x4f7ffffe, v5
	v_cvt_u32_f32_e32 v5, v5
	v_mul_lo_u32 v4, v4, v5
	v_mul_hi_u32 v4, v5, v4
	v_add_u32_e32 v4, v5, v4
	v_mul_hi_u32 v4, v3, v4
	v_mul_lo_u32 v5, v4, v2
	v_sub_u32_e32 v5, v3, v5
	v_add_u32_e32 v6, 1, v4
	v_cmp_ge_u32_e32 vcc, v5, v2
	s_nop 1
	v_cndmask_b32_e32 v4, v4, v6, vcc
	v_sub_u32_e32 v6, v5, v2
	v_cndmask_b32_e32 v5, v5, v6, vcc
	v_add_u32_e32 v6, 1, v4
	v_cmp_ge_u32_e32 vcc, v5, v2
	v_add_u32_e32 v5, 1, v3
	s_nop 0
	v_cndmask_b32_e32 v4, v4, v6, vcc
	v_add_u32_e32 v3, 1, v4
	v_mul_lo_u32 v2, v3, v2
	v_cmp_ne_u32_e32 vcc, v5, v2
	s_and_saveexec_b64 s[0:1], vcc
	s_xor_b64 s[8:9], exec, s[0:1]
	s_cbranch_execz .LBB0_407
	v_mov_b32_e32 v2, 0x7000
	global_load_dword v2, v2, s[6:7] offset:1024 sc1
	s_add_u32 s10, s6, 0x7400
	s_waitcnt lgkmcnt(0)
	v_mul_lo_u32 v0, v3, v0
	s_addc_u32 s11, s7, 0
	s_waitcnt vmcnt(0)
	v_cmp_lt_u32_e32 vcc, v2, v0
	s_and_saveexec_b64 s[12:13], vcc
	s_cbranch_execz .LBB0_406
	s_add_u32 s14, s6, 0x4200
	s_addc_u32 s15, s7, 0
	s_mov_b32 s0, 1
	s_mov_b64 s[16:17], 0
	s_branch .LBB0_397

; __device__ __forceinline__ unsigned xb_ld(unsigned* p)              { return __hip_atomic_load(p, __ATOMIC_RELAXED, __HIP_MEMORY_SCOPE_AGENT); }
; #define XB_SPIN(cond, bar) do { unsigned _sp = 0; while (cond) { __builtin_amdgcn_s_sleep(1); \
;     if ((++_sp & 255u) == 0u) { if (xb_ld(&(bar)[XB_TMO])) break; if (_sp > XB_SPIN_CAP) { atomicAdd(&(bar)[XB_TMO], 1u); break; } } } } while (0)
; __device__ __forceinline__ float* karg_out() { return (float*)(GAS float*)karg_u64<14>(); }
; __device__ __forceinline__ unsigned char* karg_ws() { return (unsigned char*)(GAS unsigned char*)karg_u64<15>(); }
; __device__ __forceinline__ void xcd_barrier_impl(const XcdBarrier& b, bool leader) {
;     ...
;             __builtin_amdgcn_fence(__ATOMIC_ACQUIRE, "agent");
;             asm volatile("s_waitcnt vmcnt(0)" ::: "memory");
;         } else {
;             XB_SPIN(xb_ld(&bar[XB_TOP]) < (gen + 1u) * nx, bar);
;             __builtin_amdgcn_fence(__ATOMIC_ACQUIRE, "agent");
;             asm volatile("s_waitcnt vmcnt(0)" ::: "memory");
;         }
;     }
;     __syncthreads();
; __global__ void __launch_bounds__(512, 2) trunk_fwd(Args args) {
;     ...
;             { unsigned char* ws = karg_ws(); float* OUT = karg_out();
;               pg8::Gemm g{(const bf16_t*)(ws + WS_OQ), (const bf16_t*)(ws + WS_W_OOUT + li * SZ_SQ), D, D, D, nullptr};
;               pg8::EpiRes E{(const float*)nullptr, (float*)nullptr, ws, false};
.LBB0_423:
	s_or_b64 exec, exec, s[10:11]
	s_waitcnt vmcnt(0)
	s_waitcnt vmcnt(0)
.LBB0_424:
	s_or_b64 exec, exec, s[4:5]
	s_waitcnt lgkmcnt(0)
	s_barrier
	s_load_dwordx2 s[6:7], s[76:77], 0x78
	s_waitcnt lgkmcnt(0)
	s_load_dwordx2 s[0:1], s[76:77], 0x70
	s_waitcnt lgkmcnt(0)
	v_readlane_b32 s2, v254, 17
	v_mbcnt_lo_u32_b32 v0, -1, 0
	v_mbcnt_hi_u32_b32 v0, -1, v0
	v_readlane_b32 s3, v254, 18
	s_waitcnt vmcnt(12)
	v_add_u32_e32 v16, s79, v0
	v_readlane_b32 s74, v254, 57
	s_and_b64 vcc, exec, s[2:3]
	v_readfirstlane_b32 s0, v16
	v_readlane_b32 s75, v254, 58
	s_cbranch_vccz .LBB0_426
	v_readlane_b32 s1, v254, 38
	s_mov_b32 s22, s1
	v_readlane_b32 s1, v254, 37
	s_mov_b32 s24, s1
